# MLA loop also unrolled x4 over its 20 KB ring (slots 2/3 addressed from bases + 0xa000 kept in the former address temporaries)
# speedup vs baseline: 1.0103x; 1.0030x over previous
.LBB0_926:
	v_lshlrev_b32_e32 v12, 10, v4
	v_and_b32_e32 v4, 19, v3
	v_lshlrev_b32_e32 v5, 1, v2
	v_lshrrev_b32_e32 v3, 1, v3
	s_add_u32 s12, s30, s25
	v_and_b32_e32 v5, 8, v5
	v_and_b32_e32 v3, 4, v3
	s_addc_u32 s13, s31, s26
	v_or3_b32 v3, v4, v5, v3
	v_lshl_add_u64 v[4:5], s[12:13], 0, v[0:1]
	v_lshl_add_u64 v[4:5], v[4:5], 0, s[52:53]
	s_add_i32 m0, s27, 0x8000
	v_lshl_or_b32 v231, v3, 4, v12
	global_load_lds_dwordx4 v[4:5], off
	v_mov_b32_e32 v178, v1
	v_add_u32_e32 v232, 0, v231
	s_waitcnt vmcnt(0)
	s_waitcnt vmcnt(0) lgkmcnt(0)
	s_barrier
	ds_read_b128 v[4:7], v232
	ds_read_b128 v[98:101], v232 offset:512
	s_waitcnt lgkmcnt(1)
	v_mfma_f32_32x32x16_bf16 v[82:97], v[4:7], v[130:133], 0
	v_lshl_or_b32 v233, v2, 4, v12
	v_mov_b32_e32 v2, 0
	s_mov_b32 s12, 1
	s_mov_b32 s33, 0
	v_add_u32_e32 v234, 0, v233
	s_mov_b32 s13, 2
	s_mov_b32 s30, 0
	v_mfma_f32_32x32x16_bf16 v[66:81], v[4:7], v[170:173], 0
	ds_read_b128 v[4:7], v232 offset:2048
	ds_read_b128 v[194:197], v232 offset:2560
	ds_read_b128 v[8:11], v232 offset:4096
	ds_read_b128 v[12:15], v232 offset:6144
	ds_read_b128 v[18:21], v232 offset:8192
	ds_read_b128 v[22:25], v232 offset:10240
	s_mov_b32 s31, 0
	v_mov_b32_e32 v179, v178
	v_mov_b32_e32 v180, v178
	v_mov_b32_e32 v181, v178
	s_waitcnt lgkmcnt(5)
	v_mfma_f32_32x32x16_bf16 v[82:97], v[4:7], v[134:137], v[82:97]
	v_mov_b32_e32 v182, v178
	v_mov_b32_e32 v183, v178
	v_mov_b32_e32 v184, v178
	v_mov_b32_e32 v185, v178
	v_mov_b32_e32 v190, v178
	v_mov_b32_e32 v191, v178
	v_mov_b32_e32 v192, v178
	v_mfma_f32_32x32x16_bf16 v[66:81], v[4:7], v[138:141], v[66:81]
	v_mov_b32_e32 v193, v178
	v_mov_b32_e32 v186, v178
	v_mov_b32_e32 v187, v178
	v_mov_b32_e32 v188, v178
	v_mov_b32_e32 v189, v178
	v_mov_b32_e32 v3, v2
	v_mov_b32_e32 v4, v2
	s_waitcnt lgkmcnt(3)
	v_mfma_f32_32x32x16_bf16 v[82:97], v[8:11], v[146:149], v[82:97]
	v_mov_b32_e32 v5, v2
	v_mov_b32_e32 v6, v2
	v_mov_b32_e32 v7, v2
	v_mov_b32_e32 v16, v2
	v_mov_b32_e32 v17, v2
	v_mov_b32_e32 v50, v2
	v_mov_b32_e32 v51, v2
	v_mfma_f32_32x32x16_bf16 v[66:81], v[8:11], v[142:145], v[66:81]
	v_mov_b32_e32 v8, v2
	v_mov_b32_e32 v9, v2
	v_mov_b32_e32 v10, v2
	v_mov_b32_e32 v11, v2
	v_mov_b32_e32 v52, v2
	v_mov_b32_e32 v53, v2
	v_mov_b32_e32 v54, v2
	s_waitcnt lgkmcnt(2)
	v_mfma_f32_32x32x16_bf16 v[82:97], v[12:15], v[150:153], v[82:97]
	v_mov_b32_e32 v55, v2
	v_mov_b32_e32 v56, v2
	v_mov_b32_e32 v57, v2
	v_mov_b32_e32 v58, v2
	v_mov_b32_e32 v59, v2
	v_mov_b32_e32 v60, v2
	v_mov_b32_e32 v61, v2
	v_mfma_f32_32x32x16_bf16 v[66:81], v[12:15], v[154:157], v[66:81]
	v_mov_b32_e32 v12, v2
	v_mov_b32_e32 v13, v2
	v_mov_b32_e32 v14, v2
	v_mov_b32_e32 v15, v2
	v_mov_b32_e32 v62, v2
	v_mov_b32_e32 v63, v2
	v_mov_b32_e32 v64, v2
	s_waitcnt lgkmcnt(1)
	v_mfma_f32_32x32x16_bf16 v[82:97], v[18:21], v[162:165], v[82:97]
	v_mov_b32_e32 v65, v2
	v_mov_b32_e32 v34, v2
	v_mov_b32_e32 v35, v2
	v_mov_b32_e32 v36, v2
	v_mov_b32_e32 v37, v2
	v_mov_b32_e32 v38, v2
	v_mov_b32_e32 v39, v2
	v_mfma_f32_32x32x16_bf16 v[66:81], v[18:21], v[158:161], v[66:81]
	v_mov_b32_e32 v40, v2
	v_mov_b32_e32 v41, v2
	v_mov_b32_e32 v42, v2
	v_mov_b32_e32 v43, v2
	v_mov_b32_e32 v44, v2
	v_mov_b32_e32 v45, v2
	v_mov_b32_e32 v46, v2
	s_waitcnt lgkmcnt(0)
	v_mfma_f32_32x32x16_bf16 v[82:97], v[22:25], v[166:169], v[82:97]
	v_mov_b32_e32 v47, v2
	v_mov_b32_e32 v48, v2
	v_mov_b32_e32 v49, v2
	v_mov_b32_e32 v18, v2
	v_mov_b32_e32 v19, v2
	v_mov_b32_e32 v20, v2
	v_mov_b32_e32 v21, v2
	v_mfma_f32_32x32x16_bf16 v[66:81], v[22:25], v[174:177], v[66:81]
	v_mov_b32_e32 v22, v2
	v_mov_b32_e32 v23, v2
	v_mov_b32_e32 v24, v2
	v_mov_b32_e32 v25, v2
	v_mov_b32_e32 v26, v2
	v_mov_b32_e32 v27, v2
	v_mov_b32_e32 v28, v2
	v_mov_b32_e32 v29, v2
	v_mov_b32_e32 v30, v2
	v_mov_b32_e32 v31, v2
	v_mov_b32_e32 v32, v2
	v_mov_b32_e32 v33, v2
	v_mov_b32_e32 v202, v2
	v_mov_b32_e32 v203, v2
	v_mov_b32_e32 v212, v202
	v_mov_b32_e32 v213, v203
	s_waitcnt lgkmcnt(0)
	v_mov_b32_e32 v240, v98
	v_mov_b32_e32 v241, v99
	v_mov_b32_e32 v242, v100
	v_mov_b32_e32 v243, v101
	v_mov_b32_e32 v244, v194
	v_mov_b32_e32 v245, v195
	v_mov_b32_e32 v246, v196
	v_mov_b32_e32 v247, v197
	v_add_u32_e32 v224, 0xa000, v231
	v_add_u32_e32 v214, 0xa000, v233
	v_add_u32_e32 v210, 0xa000, v232
	v_add_u32_e32 v215, 0xa000, v234
.LBB0_927:
	s_min_i32 s34, s31, 0x101
	s_add_i32 s88, s34, 2
	s_mul_i32 s34, s88, 0x3000
	s_add_u32 s35, s22, s34
	s_addc_u32 s38, s23, 0
	s_add_u32 s40, s35, s25
	s_addc_u32 s41, s38, s26
	s_add_i32 s34, s27, 0xa000
	s_mov_b32 m0, s34
	s_andn2_b64 vcc, exec, s[10:11]
	global_load_lds_dwordx4 v0, s[40:41]
	s_cbranch_vccnz .Lmla929_0
	s_add_u32 s40, s35, s28
	s_addc_u32 s41, s38, s29
	s_add_i32 m0, s34, 0x2000
	s_nop 0
	global_load_lds_dwordx4 v0, s[40:41]
.Lmla929_0:
	s_lshl_b64 s[38:39], s[88:89], 13
	s_add_i32 m0, s34, 0x3000
	s_add_u32 s60, s56, s38
	s_addc_u32 s61, s57, s39
	global_load_lds_dwordx4 v0, s[60:61]
	s_mul_i32 s35, s33, 0x5000
	v_add_u32_e32 v225, s35, v234
	ds_read_b128 v[216:219], v231 offset:4608
	v_mfma_f32_32x32x16_bf16 v[114:129], v[240:243], v[130:133], 0
	v_exp_f32_e32 v82, v82
	v_exp_f32_e32 v83, v83
	v_exp_f32_e32 v84, v84
	v_mfma_f32_32x32x16_bf16 v[98:113], v[240:243], v[170:173], 0
	ds_read_b128 v[220:223], v231 offset:6656
	v_exp_f32_e32 v85, v85
	v_cvt_pk_bf16_f32 v198, v82, v83
	v_add_f32_e32 v212, v82, v212
	v_add_f32_e32 v212, v83, v212
	v_mfma_f32_32x32x16_bf16 v[114:129], v[244:247], v[134:137], v[114:129]
	v_exp_f32_e32 v86, v86
	v_exp_f32_e32 v87, v87
	v_cvt_pk_bf16_f32 v199, v84, v85
	v_add_f32_e32 v212, v84, v212
	v_mfma_f32_32x32x16_bf16 v[98:113], v[244:247], v[138:141], v[98:113]
	ds_read_b128 v[240:243], v231 offset:8704
	v_add_f32_e32 v212, v85, v212
	v_exp_f32_e32 v88, v88
	v_exp_f32_e32 v89, v89
	s_waitcnt lgkmcnt(2)
	v_mfma_f32_32x32x16_bf16 v[114:129], v[216:219], v[146:149], v[114:129]
	v_cvt_pk_bf16_f32 v200, v86, v87
	v_add_f32_e32 v212, v86, v212
	v_add_f32_e32 v212, v87, v212
	v_exp_f32_e32 v90, v90
	v_exp_f32_e32 v91, v91
	v_mfma_f32_32x32x16_bf16 v[98:113], v[216:219], v[142:145], v[98:113]
	ds_read_b128 v[244:247], v231 offset:10752
	v_cvt_pk_bf16_f32 v201, v88, v89
	v_add_f32_e32 v212, v88, v212
	v_add_f32_e32 v212, v89, v212
	v_exp_f32_e32 v92, v92
	s_waitcnt lgkmcnt(2)
	v_mfma_f32_32x32x16_bf16 v[114:129], v[220:223], v[150:153], v[114:129]
	v_exp_f32_e32 v93, v93
	v_cvt_pk_bf16_f32 v194, v90, v91
	v_add_f32_e32 v212, v90, v212
	v_add_f32_e32 v212, v91, v212
	v_mfma_f32_32x32x16_bf16 v[98:113], v[220:223], v[154:157], v[98:113]
	ds_read_b128 v[216:219], v225 offset:16384
	v_exp_f32_e32 v94, v94
	v_exp_f32_e32 v95, v95
	v_cvt_pk_bf16_f32 v195, v92, v93
	v_add_f32_e32 v212, v92, v212
	s_waitcnt lgkmcnt(2)
	v_mfma_f32_32x32x16_bf16 v[114:129], v[240:243], v[162:165], v[114:129]
	v_add_f32_e32 v212, v93, v212
	v_exp_f32_e32 v96, v96
	v_exp_f32_e32 v97, v97
	v_mfma_f32_32x32x16_bf16 v[98:113], v[240:243], v[158:161], v[98:113]
	ds_read_b128 v[220:223], v225 offset:16896
	v_cvt_pk_bf16_f32 v196, v94, v95
	v_add_f32_e32 v212, v94, v212
	v_add_f32_e32 v212, v95, v212
	v_exp_f32_e32 v66, v66
	v_exp_f32_e32 v67, v67
	s_waitcnt lgkmcnt(2)
	v_mfma_f32_32x32x16_bf16 v[114:129], v[244:247], v[166:169], v[114:129]
	v_cvt_pk_bf16_f32 v197, v96, v97
	v_add_f32_e32 v212, v96, v212
	v_add_f32_e32 v212, v97, v212
	v_exp_f32_e32 v68, v68
	v_mfma_f32_32x32x16_bf16 v[98:113], v[244:247], v[174:177], v[98:113]
	v_exp_f32_e32 v69, v69
	v_cvt_pk_bf16_f32 v202, v66, v67
	v_add_f32_e32 v213, v66, v213
	v_add_f32_e32 v213, v67, v213
	s_waitcnt lgkmcnt(1)
	v_mfma_f32_32x32x16_bf16 v[18:33], v[216:219], v[178:181], v[18:33]
	ds_read_b128 v[240:243], v225 offset:18432
	v_exp_f32_e32 v70, v70
	v_exp_f32_e32 v71, v71
	v_cvt_pk_bf16_f32 v203, v68, v69
	v_add_f32_e32 v213, v68, v213
	s_waitcnt lgkmcnt(1)
	v_mfma_f32_32x32x16_bf16 v[34:49], v[220:223], v[178:181], v[34:49]
	ds_read_b128 v[244:247], v225 offset:18944
	v_add_f32_e32 v213, v69, v213
	v_exp_f32_e32 v72, v72
	v_exp_f32_e32 v73, v73
	v_mfma_f32_32x32x16_bf16 v[50:65], v[216:219], v[190:193], v[50:65]
	v_cvt_pk_bf16_f32 v204, v70, v71
	v_add_f32_e32 v213, v70, v213
	v_add_f32_e32 v213, v71, v213
	v_exp_f32_e32 v74, v74
	v_exp_f32_e32 v75, v75
	v_mfma_f32_32x32x16_bf16 v[2:17], v[220:223], v[190:193], v[2:17]
	v_cvt_pk_bf16_f32 v205, v72, v73
	v_add_f32_e32 v213, v72, v213
	v_add_f32_e32 v213, v73, v213
	v_exp_f32_e32 v76, v76
	s_waitcnt lgkmcnt(1)
	v_mfma_f32_32x32x16_bf16 v[18:33], v[240:243], v[182:185], v[18:33]
	ds_read_b128 v[216:219], v232 offset:20480
	v_exp_f32_e32 v77, v77
	v_cvt_pk_bf16_f32 v206, v74, v75
	v_add_f32_e32 v213, v74, v213
	v_add_f32_e32 v213, v75, v213
	s_waitcnt lgkmcnt(1)
	v_mfma_f32_32x32x16_bf16 v[34:49], v[244:247], v[182:185], v[34:49]
	v_exp_f32_e32 v78, v78
	v_exp_f32_e32 v79, v79
	v_cvt_pk_bf16_f32 v207, v76, v77
	v_add_f32_e32 v213, v76, v213
	v_mfma_f32_32x32x16_bf16 v[50:65], v[240:243], v[186:189], v[50:65]
	ds_read_b128 v[220:223], v232 offset:22528
	v_add_f32_e32 v213, v77, v213
	v_exp_f32_e32 v80, v80
	v_exp_f32_e32 v81, v81
	v_mfma_f32_32x32x16_bf16 v[2:17], v[244:247], v[186:189], v[2:17]
	v_cvt_pk_bf16_f32 v208, v78, v79
	v_add_f32_e32 v213, v78, v213
	v_add_f32_e32 v213, v79, v213
	v_cvt_pk_bf16_f32 v209, v80, v81
	v_add_f32_e32 v213, v80, v213
	v_add_f32_e32 v213, v81, v213
	s_waitcnt lgkmcnt(1)
	v_mfma_f32_32x32x16_bf16 v[82:97], v[216:219], v[130:133], 0
	ds_read_b128 v[240:243], v232 offset:24576
	v_exp_f32_e32 v114, v114
	v_exp_f32_e32 v115, v115
	v_exp_f32_e32 v116, v116
	v_mfma_f32_32x32x16_bf16 v[66:81], v[216:219], v[170:173], 0
	v_exp_f32_e32 v117, v117
	v_cvt_pk_bf16_f32 v178, v114, v115
	v_add_f32_e32 v212, v114, v212
	v_add_f32_e32 v212, v115, v212
	s_waitcnt lgkmcnt(1)
	v_mfma_f32_32x32x16_bf16 v[82:97], v[220:223], v[134:137], v[82:97]
	ds_read_b128 v[244:247], v232 offset:26624
	v_exp_f32_e32 v118, v118
	v_exp_f32_e32 v119, v119
	v_cvt_pk_bf16_f32 v179, v116, v117
	v_add_f32_e32 v212, v116, v212
	v_mfma_f32_32x32x16_bf16 v[66:81], v[220:223], v[138:141], v[66:81]
	v_add_f32_e32 v212, v117, v212
	v_exp_f32_e32 v120, v120
	v_exp_f32_e32 v121, v121
	s_waitcnt lgkmcnt(1)
	v_mfma_f32_32x32x16_bf16 v[82:97], v[240:243], v[146:149], v[82:97]
	ds_read_b128 v[216:219], v232 offset:28672
	v_cvt_pk_bf16_f32 v180, v118, v119
	v_add_f32_e32 v212, v118, v212
	v_add_f32_e32 v212, v119, v212
	v_exp_f32_e32 v122, v122
	v_exp_f32_e32 v123, v123
	v_mfma_f32_32x32x16_bf16 v[66:81], v[240:243], v[142:145], v[66:81]
	v_cvt_pk_bf16_f32 v181, v120, v121
	v_add_f32_e32 v212, v120, v212
	v_add_f32_e32 v212, v121, v212
	v_exp_f32_e32 v124, v124
	s_waitcnt lgkmcnt(1)
	v_mfma_f32_32x32x16_bf16 v[82:97], v[244:247], v[150:153], v[82:97]
	ds_read_b128 v[220:223], v232 offset:30720
	v_exp_f32_e32 v125, v125
	v_cvt_pk_bf16_f32 v182, v122, v123
	v_add_f32_e32 v212, v122, v212
	v_add_f32_e32 v212, v123, v212
	v_mfma_f32_32x32x16_bf16 v[66:81], v[244:247], v[154:157], v[66:81]
	v_exp_f32_e32 v126, v126
	v_exp_f32_e32 v127, v127
	v_cvt_pk_bf16_f32 v183, v124, v125
	v_add_f32_e32 v212, v124, v212
	s_waitcnt lgkmcnt(1)
	v_mfma_f32_32x32x16_bf16 v[82:97], v[216:219], v[162:165], v[82:97]
	ds_read_b128 v[240:243], v233 offset:12288
	v_add_f32_e32 v212, v125, v212
	v_exp_f32_e32 v128, v128
	v_exp_f32_e32 v129, v129
	v_mfma_f32_32x32x16_bf16 v[66:81], v[216:219], v[158:161], v[66:81]
	ds_read_b128 v[244:247], v233 offset:12800
	v_cvt_pk_bf16_f32 v184, v126, v127
	v_add_f32_e32 v212, v126, v212
	v_add_f32_e32 v212, v127, v212
	v_exp_f32_e32 v98, v98
	v_exp_f32_e32 v99, v99
	s_waitcnt lgkmcnt(2)
	v_mfma_f32_32x32x16_bf16 v[82:97], v[220:223], v[166:169], v[82:97]
	v_cvt_pk_bf16_f32 v185, v128, v129
	v_add_f32_e32 v212, v128, v212
	v_add_f32_e32 v212, v129, v212
	v_exp_f32_e32 v100, v100
	v_mfma_f32_32x32x16_bf16 v[66:81], v[220:223], v[174:177], v[66:81]
	v_exp_f32_e32 v101, v101
	v_cvt_pk_bf16_f32 v190, v98, v99
	v_add_f32_e32 v213, v98, v213
	v_add_f32_e32 v213, v99, v213
	s_waitcnt lgkmcnt(1)
	v_mfma_f32_32x32x16_bf16 v[18:33], v[240:243], v[198:201], v[18:33]
	ds_read_b128 v[216:219], v233 offset:14336
	v_exp_f32_e32 v102, v102
	v_exp_f32_e32 v103, v103
	v_cvt_pk_bf16_f32 v191, v100, v101
	v_add_f32_e32 v213, v100, v213
	s_waitcnt lgkmcnt(1)
	v_mfma_f32_32x32x16_bf16 v[34:49], v[244:247], v[198:201], v[34:49]
	ds_read_b128 v[220:223], v233 offset:14848
	v_add_f32_e32 v213, v101, v213
	v_exp_f32_e32 v104, v104
	v_exp_f32_e32 v105, v105
	v_mfma_f32_32x32x16_bf16 v[50:65], v[240:243], v[202:205], v[50:65]
	v_cvt_pk_bf16_f32 v192, v102, v103
	v_add_f32_e32 v213, v102, v213
	v_add_f32_e32 v213, v103, v213
	v_exp_f32_e32 v106, v106
	v_exp_f32_e32 v107, v107
	v_mfma_f32_32x32x16_bf16 v[2:17], v[244:247], v[202:205], v[2:17]
	v_cvt_pk_bf16_f32 v193, v104, v105
	v_add_f32_e32 v213, v104, v213
	v_add_f32_e32 v213, v105, v213
	v_exp_f32_e32 v108, v108
	s_waitcnt lgkmcnt(1)
	v_mfma_f32_32x32x16_bf16 v[18:33], v[216:219], v[194:197], v[18:33]
	ds_read_b128 v[240:243], v232 offset:20992
	v_exp_f32_e32 v109, v109
	v_cvt_pk_bf16_f32 v186, v106, v107
	v_add_f32_e32 v213, v106, v213
	v_add_f32_e32 v213, v107, v213
	s_waitcnt lgkmcnt(1)
	v_mfma_f32_32x32x16_bf16 v[34:49], v[220:223], v[194:197], v[34:49]
	v_exp_f32_e32 v110, v110
	v_exp_f32_e32 v111, v111
	v_cvt_pk_bf16_f32 v187, v108, v109
	v_add_f32_e32 v213, v108, v213
	v_mfma_f32_32x32x16_bf16 v[50:65], v[216:219], v[206:209], v[50:65]
	ds_read_b128 v[244:247], v232 offset:23040
	v_add_f32_e32 v213, v109, v213
	v_exp_f32_e32 v112, v112
	v_exp_f32_e32 v113, v113
	v_mfma_f32_32x32x16_bf16 v[2:17], v[220:223], v[206:209], v[2:17]
	v_cvt_pk_bf16_f32 v188, v110, v111
	v_add_f32_e32 v213, v110, v213
	v_add_f32_e32 v213, v111, v213
	v_cvt_pk_bf16_f32 v189, v112, v113
	v_add_f32_e32 v213, v112, v213
	v_add_f32_e32 v213, v113, v213
	s_waitcnt vmcnt(0)
	s_add_i32 s31, s31, 1
	s_waitcnt vmcnt(0) lgkmcnt(0)
	s_barrier
	s_min_i32 s34, s31, 0x101
	s_add_i32 s88, s34, 2
	s_mul_i32 s34, s88, 0x3000
	s_add_u32 s35, s22, s34
	s_addc_u32 s38, s23, 0
	s_add_u32 s40, s35, s25
	s_addc_u32 s41, s38, s26
	s_add_i32 s34, s27, 0xf000
	s_mov_b32 m0, s34
	s_andn2_b64 vcc, exec, s[10:11]
	global_load_lds_dwordx4 v0, s[40:41]
	s_cbranch_vccnz .Lmla929_1
	s_add_u32 s40, s35, s28
	s_addc_u32 s41, s38, s29
	s_add_i32 m0, s34, 0x2000
	s_nop 0
	global_load_lds_dwordx4 v0, s[40:41]
.Lmla929_1:
	s_lshl_b64 s[38:39], s[88:89], 13
	s_add_i32 m0, s34, 0x3000
	s_add_u32 s60, s56, s38
	s_addc_u32 s61, s57, s39
	global_load_lds_dwordx4 v0, s[60:61]
	ds_read_b128 v[216:219], v231 offset:25088
	v_mfma_f32_32x32x16_bf16 v[114:129], v[240:243], v[130:133], 0
	v_exp_f32_e32 v82, v82
	v_exp_f32_e32 v83, v83
	v_exp_f32_e32 v84, v84
	v_mfma_f32_32x32x16_bf16 v[98:113], v[240:243], v[170:173], 0
	ds_read_b128 v[220:223], v231 offset:27136
	v_exp_f32_e32 v85, v85
	v_cvt_pk_bf16_f32 v198, v82, v83
	v_add_f32_e32 v212, v82, v212
	v_add_f32_e32 v212, v83, v212
	v_mfma_f32_32x32x16_bf16 v[114:129], v[244:247], v[134:137], v[114:129]
	v_exp_f32_e32 v86, v86
	v_exp_f32_e32 v87, v87
	v_cvt_pk_bf16_f32 v199, v84, v85
	v_add_f32_e32 v212, v84, v212
	v_mfma_f32_32x32x16_bf16 v[98:113], v[244:247], v[138:141], v[98:113]
	ds_read_b128 v[240:243], v231 offset:29184
	v_add_f32_e32 v212, v85, v212
	v_exp_f32_e32 v88, v88
	v_exp_f32_e32 v89, v89
	s_waitcnt lgkmcnt(2)
	v_mfma_f32_32x32x16_bf16 v[114:129], v[216:219], v[146:149], v[114:129]
	v_cvt_pk_bf16_f32 v200, v86, v87
	v_add_f32_e32 v212, v86, v212
	v_add_f32_e32 v212, v87, v212
	v_exp_f32_e32 v90, v90
	v_exp_f32_e32 v91, v91
	v_mfma_f32_32x32x16_bf16 v[98:113], v[216:219], v[142:145], v[98:113]
	ds_read_b128 v[244:247], v231 offset:31232
	v_cvt_pk_bf16_f32 v201, v88, v89
	v_add_f32_e32 v212, v88, v212
	v_add_f32_e32 v212, v89, v212
	v_exp_f32_e32 v92, v92
	s_waitcnt lgkmcnt(2)
	v_mfma_f32_32x32x16_bf16 v[114:129], v[220:223], v[150:153], v[114:129]
	v_exp_f32_e32 v93, v93
	v_cvt_pk_bf16_f32 v194, v90, v91
	v_add_f32_e32 v212, v90, v212
	v_add_f32_e32 v212, v91, v212
	v_mfma_f32_32x32x16_bf16 v[98:113], v[220:223], v[154:157], v[98:113]
	ds_read_b128 v[216:219], v234 offset:16384
	v_exp_f32_e32 v94, v94
	v_exp_f32_e32 v95, v95
	v_cvt_pk_bf16_f32 v195, v92, v93
	v_add_f32_e32 v212, v92, v212
	s_waitcnt lgkmcnt(2)
	v_mfma_f32_32x32x16_bf16 v[114:129], v[240:243], v[162:165], v[114:129]
	v_add_f32_e32 v212, v93, v212
	v_exp_f32_e32 v96, v96
	v_exp_f32_e32 v97, v97
	v_mfma_f32_32x32x16_bf16 v[98:113], v[240:243], v[158:161], v[98:113]
	ds_read_b128 v[220:223], v234 offset:16896
	v_cvt_pk_bf16_f32 v196, v94, v95
	v_add_f32_e32 v212, v94, v212
	v_add_f32_e32 v212, v95, v212
	v_exp_f32_e32 v66, v66
	v_exp_f32_e32 v67, v67
	s_waitcnt lgkmcnt(2)
	v_mfma_f32_32x32x16_bf16 v[114:129], v[244:247], v[166:169], v[114:129]
	v_cvt_pk_bf16_f32 v197, v96, v97
	v_add_f32_e32 v212, v96, v212
	v_add_f32_e32 v212, v97, v212
	v_exp_f32_e32 v68, v68
	v_mfma_f32_32x32x16_bf16 v[98:113], v[244:247], v[174:177], v[98:113]
	v_exp_f32_e32 v69, v69
	v_cvt_pk_bf16_f32 v202, v66, v67
	v_add_f32_e32 v213, v66, v213
	v_add_f32_e32 v213, v67, v213
	s_waitcnt lgkmcnt(1)
	v_mfma_f32_32x32x16_bf16 v[18:33], v[216:219], v[178:181], v[18:33]
	ds_read_b128 v[240:243], v234 offset:18432
	v_exp_f32_e32 v70, v70
	v_exp_f32_e32 v71, v71
	v_cvt_pk_bf16_f32 v203, v68, v69
	v_add_f32_e32 v213, v68, v213
	s_waitcnt lgkmcnt(1)
	v_mfma_f32_32x32x16_bf16 v[34:49], v[220:223], v[178:181], v[34:49]
	ds_read_b128 v[244:247], v234 offset:18944
	v_add_f32_e32 v213, v69, v213
	v_exp_f32_e32 v72, v72
	v_exp_f32_e32 v73, v73
	v_mfma_f32_32x32x16_bf16 v[50:65], v[216:219], v[190:193], v[50:65]
	v_cvt_pk_bf16_f32 v204, v70, v71
	v_add_f32_e32 v213, v70, v213
	v_add_f32_e32 v213, v71, v213
	v_exp_f32_e32 v74, v74
	v_exp_f32_e32 v75, v75
	v_mfma_f32_32x32x16_bf16 v[2:17], v[220:223], v[190:193], v[2:17]
	v_cvt_pk_bf16_f32 v205, v72, v73
	v_add_f32_e32 v213, v72, v213
	v_add_f32_e32 v213, v73, v213
	v_exp_f32_e32 v76, v76
	s_waitcnt lgkmcnt(1)
	v_mfma_f32_32x32x16_bf16 v[18:33], v[240:243], v[182:185], v[18:33]
	ds_read_b128 v[216:219], v210 offset:0
	v_exp_f32_e32 v77, v77
	v_cvt_pk_bf16_f32 v206, v74, v75
	v_add_f32_e32 v213, v74, v213
	v_add_f32_e32 v213, v75, v213
	s_waitcnt lgkmcnt(1)
	v_mfma_f32_32x32x16_bf16 v[34:49], v[244:247], v[182:185], v[34:49]
	v_exp_f32_e32 v78, v78
	v_exp_f32_e32 v79, v79
	v_cvt_pk_bf16_f32 v207, v76, v77
	v_add_f32_e32 v213, v76, v213
	v_mfma_f32_32x32x16_bf16 v[50:65], v[240:243], v[186:189], v[50:65]
	ds_read_b128 v[220:223], v210 offset:2048
	v_add_f32_e32 v213, v77, v213
	v_exp_f32_e32 v80, v80
	v_exp_f32_e32 v81, v81
	v_mfma_f32_32x32x16_bf16 v[2:17], v[244:247], v[186:189], v[2:17]
	v_cvt_pk_bf16_f32 v208, v78, v79
	v_add_f32_e32 v213, v78, v213
	v_add_f32_e32 v213, v79, v213
	v_cvt_pk_bf16_f32 v209, v80, v81
	v_add_f32_e32 v213, v80, v213
	v_add_f32_e32 v213, v81, v213
	s_waitcnt lgkmcnt(1)
	v_mfma_f32_32x32x16_bf16 v[82:97], v[216:219], v[130:133], 0
	ds_read_b128 v[240:243], v210 offset:4096
	v_exp_f32_e32 v114, v114
	v_exp_f32_e32 v115, v115
	v_exp_f32_e32 v116, v116
	v_mfma_f32_32x32x16_bf16 v[66:81], v[216:219], v[170:173], 0
	v_exp_f32_e32 v117, v117
	v_cvt_pk_bf16_f32 v178, v114, v115
	v_add_f32_e32 v212, v114, v212
	v_add_f32_e32 v212, v115, v212
	s_waitcnt lgkmcnt(1)
	v_mfma_f32_32x32x16_bf16 v[82:97], v[220:223], v[134:137], v[82:97]
	ds_read_b128 v[244:247], v210 offset:6144
	v_exp_f32_e32 v118, v118
	v_exp_f32_e32 v119, v119
	v_cvt_pk_bf16_f32 v179, v116, v117
	v_add_f32_e32 v212, v116, v212
	v_mfma_f32_32x32x16_bf16 v[66:81], v[220:223], v[138:141], v[66:81]
	v_add_f32_e32 v212, v117, v212
	v_exp_f32_e32 v120, v120
	v_exp_f32_e32 v121, v121
	s_waitcnt lgkmcnt(1)
	v_mfma_f32_32x32x16_bf16 v[82:97], v[240:243], v[146:149], v[82:97]
	ds_read_b128 v[216:219], v210 offset:8192
	v_cvt_pk_bf16_f32 v180, v118, v119
	v_add_f32_e32 v212, v118, v212
	v_add_f32_e32 v212, v119, v212
	v_exp_f32_e32 v122, v122
	v_exp_f32_e32 v123, v123
	v_mfma_f32_32x32x16_bf16 v[66:81], v[240:243], v[142:145], v[66:81]
	v_cvt_pk_bf16_f32 v181, v120, v121
	v_add_f32_e32 v212, v120, v212
	v_add_f32_e32 v212, v121, v212
	v_exp_f32_e32 v124, v124
	s_waitcnt lgkmcnt(1)
	v_mfma_f32_32x32x16_bf16 v[82:97], v[244:247], v[150:153], v[82:97]
	ds_read_b128 v[220:223], v210 offset:10240
	v_exp_f32_e32 v125, v125
	v_cvt_pk_bf16_f32 v182, v122, v123
	v_add_f32_e32 v212, v122, v212
	v_add_f32_e32 v212, v123, v212
	v_mfma_f32_32x32x16_bf16 v[66:81], v[244:247], v[154:157], v[66:81]
	v_exp_f32_e32 v126, v126
	v_exp_f32_e32 v127, v127
	v_cvt_pk_bf16_f32 v183, v124, v125
	v_add_f32_e32 v212, v124, v212
	s_waitcnt lgkmcnt(1)
	v_mfma_f32_32x32x16_bf16 v[82:97], v[216:219], v[162:165], v[82:97]
	ds_read_b128 v[240:243], v233 offset:32768
	v_add_f32_e32 v212, v125, v212
	v_exp_f32_e32 v128, v128
	v_exp_f32_e32 v129, v129
	v_mfma_f32_32x32x16_bf16 v[66:81], v[216:219], v[158:161], v[66:81]
	ds_read_b128 v[244:247], v233 offset:33280
	v_cvt_pk_bf16_f32 v184, v126, v127
	v_add_f32_e32 v212, v126, v212
	v_add_f32_e32 v212, v127, v212
	v_exp_f32_e32 v98, v98
	v_exp_f32_e32 v99, v99
	s_waitcnt lgkmcnt(2)
	v_mfma_f32_32x32x16_bf16 v[82:97], v[220:223], v[166:169], v[82:97]
	v_cvt_pk_bf16_f32 v185, v128, v129
	v_add_f32_e32 v212, v128, v212
	v_add_f32_e32 v212, v129, v212
	v_exp_f32_e32 v100, v100
	v_mfma_f32_32x32x16_bf16 v[66:81], v[220:223], v[174:177], v[66:81]
	v_exp_f32_e32 v101, v101
	v_cvt_pk_bf16_f32 v190, v98, v99
	v_add_f32_e32 v213, v98, v213
	v_add_f32_e32 v213, v99, v213
	s_waitcnt lgkmcnt(1)
	v_mfma_f32_32x32x16_bf16 v[18:33], v[240:243], v[198:201], v[18:33]
	ds_read_b128 v[216:219], v233 offset:34816
	v_exp_f32_e32 v102, v102
	v_exp_f32_e32 v103, v103
	v_cvt_pk_bf16_f32 v191, v100, v101
	v_add_f32_e32 v213, v100, v213
	s_waitcnt lgkmcnt(1)
	v_mfma_f32_32x32x16_bf16 v[34:49], v[244:247], v[198:201], v[34:49]
	ds_read_b128 v[220:223], v233 offset:35328
	v_add_f32_e32 v213, v101, v213
	v_exp_f32_e32 v104, v104
	v_exp_f32_e32 v105, v105
	v_mfma_f32_32x32x16_bf16 v[50:65], v[240:243], v[202:205], v[50:65]
	v_cvt_pk_bf16_f32 v192, v102, v103
	v_add_f32_e32 v213, v102, v213
	v_add_f32_e32 v213, v103, v213
	v_exp_f32_e32 v106, v106
	v_exp_f32_e32 v107, v107
	v_mfma_f32_32x32x16_bf16 v[2:17], v[244:247], v[202:205], v[2:17]
	v_cvt_pk_bf16_f32 v193, v104, v105
	v_add_f32_e32 v213, v104, v213
	v_add_f32_e32 v213, v105, v213
	v_exp_f32_e32 v108, v108
	s_waitcnt lgkmcnt(1)
	v_mfma_f32_32x32x16_bf16 v[18:33], v[216:219], v[194:197], v[18:33]
	ds_read_b128 v[240:243], v210 offset:512
	v_exp_f32_e32 v109, v109
	v_cvt_pk_bf16_f32 v186, v106, v107
	v_add_f32_e32 v213, v106, v213
	v_add_f32_e32 v213, v107, v213
	s_waitcnt lgkmcnt(1)
	v_mfma_f32_32x32x16_bf16 v[34:49], v[220:223], v[194:197], v[34:49]
	v_exp_f32_e32 v110, v110
	v_exp_f32_e32 v111, v111
	v_cvt_pk_bf16_f32 v187, v108, v109
	v_add_f32_e32 v213, v108, v213
	v_mfma_f32_32x32x16_bf16 v[50:65], v[216:219], v[206:209], v[50:65]
	ds_read_b128 v[244:247], v210 offset:2560
	v_add_f32_e32 v213, v109, v213
	v_exp_f32_e32 v112, v112
	v_exp_f32_e32 v113, v113
	v_mfma_f32_32x32x16_bf16 v[2:17], v[220:223], v[206:209], v[2:17]
	v_cvt_pk_bf16_f32 v188, v110, v111
	v_add_f32_e32 v213, v110, v213
	v_add_f32_e32 v213, v111, v213
	v_cvt_pk_bf16_f32 v189, v112, v113
	v_add_f32_e32 v213, v112, v213
	v_add_f32_e32 v213, v113, v213
	s_waitcnt vmcnt(0)
	s_add_i32 s31, s31, 1
	s_waitcnt vmcnt(0) lgkmcnt(0)
	s_barrier
	s_min_i32 s34, s31, 0x101
	s_add_i32 s88, s34, 2
	s_mul_i32 s34, s88, 0x3000
	s_add_u32 s35, s22, s34
	s_addc_u32 s38, s23, 0
	s_add_u32 s40, s35, s25
	s_addc_u32 s41, s38, s26
	s_add_i32 s34, s27, 0x0
	s_mov_b32 m0, s34
	s_andn2_b64 vcc, exec, s[10:11]
	global_load_lds_dwordx4 v0, s[40:41]
	s_cbranch_vccnz .Lmla929_2
	s_add_u32 s40, s35, s28
	s_addc_u32 s41, s38, s29
	s_add_i32 m0, s34, 0x2000
	s_nop 0
	global_load_lds_dwordx4 v0, s[40:41]
.Lmla929_2:
	s_lshl_b64 s[38:39], s[88:89], 13
	s_add_i32 m0, s34, 0x3000
	s_add_u32 s60, s56, s38
	s_addc_u32 s61, s57, s39
	global_load_lds_dwordx4 v0, s[60:61]
	ds_read_b128 v[216:219], v224 offset:4608
	v_mfma_f32_32x32x16_bf16 v[114:129], v[240:243], v[130:133], 0
	v_exp_f32_e32 v82, v82
	v_exp_f32_e32 v83, v83
	v_exp_f32_e32 v84, v84
	v_mfma_f32_32x32x16_bf16 v[98:113], v[240:243], v[170:173], 0
	ds_read_b128 v[220:223], v224 offset:6656
	v_exp_f32_e32 v85, v85
	v_cvt_pk_bf16_f32 v198, v82, v83
	v_add_f32_e32 v212, v82, v212
	v_add_f32_e32 v212, v83, v212
	v_mfma_f32_32x32x16_bf16 v[114:129], v[244:247], v[134:137], v[114:129]
	v_exp_f32_e32 v86, v86
	v_exp_f32_e32 v87, v87
	v_cvt_pk_bf16_f32 v199, v84, v85
	v_add_f32_e32 v212, v84, v212
	v_mfma_f32_32x32x16_bf16 v[98:113], v[244:247], v[138:141], v[98:113]
	ds_read_b128 v[240:243], v224 offset:8704
	v_add_f32_e32 v212, v85, v212
	v_exp_f32_e32 v88, v88
	v_exp_f32_e32 v89, v89
	s_waitcnt lgkmcnt(2)
	v_mfma_f32_32x32x16_bf16 v[114:129], v[216:219], v[146:149], v[114:129]
	v_cvt_pk_bf16_f32 v200, v86, v87
	v_add_f32_e32 v212, v86, v212
	v_add_f32_e32 v212, v87, v212
	v_exp_f32_e32 v90, v90
	v_exp_f32_e32 v91, v91
	v_mfma_f32_32x32x16_bf16 v[98:113], v[216:219], v[142:145], v[98:113]
	ds_read_b128 v[244:247], v224 offset:10752
	v_cvt_pk_bf16_f32 v201, v88, v89
	v_add_f32_e32 v212, v88, v212
	v_add_f32_e32 v212, v89, v212
	v_exp_f32_e32 v92, v92
	s_waitcnt lgkmcnt(2)
	v_mfma_f32_32x32x16_bf16 v[114:129], v[220:223], v[150:153], v[114:129]
	v_exp_f32_e32 v93, v93
	v_cvt_pk_bf16_f32 v194, v90, v91
	v_add_f32_e32 v212, v90, v212
	v_add_f32_e32 v212, v91, v212
	v_mfma_f32_32x32x16_bf16 v[98:113], v[220:223], v[154:157], v[98:113]
	ds_read_b128 v[216:219], v234 offset:36864
	v_exp_f32_e32 v94, v94
	v_exp_f32_e32 v95, v95
	v_cvt_pk_bf16_f32 v195, v92, v93
	v_add_f32_e32 v212, v92, v212
	s_waitcnt lgkmcnt(2)
	v_mfma_f32_32x32x16_bf16 v[114:129], v[240:243], v[162:165], v[114:129]
	v_add_f32_e32 v212, v93, v212
	v_exp_f32_e32 v96, v96
	v_exp_f32_e32 v97, v97
	v_mfma_f32_32x32x16_bf16 v[98:113], v[240:243], v[158:161], v[98:113]
	ds_read_b128 v[220:223], v234 offset:37376
	v_cvt_pk_bf16_f32 v196, v94, v95
	v_add_f32_e32 v212, v94, v212
	v_add_f32_e32 v212, v95, v212
	v_exp_f32_e32 v66, v66
	v_exp_f32_e32 v67, v67
	s_waitcnt lgkmcnt(2)
	v_mfma_f32_32x32x16_bf16 v[114:129], v[244:247], v[166:169], v[114:129]
	v_cvt_pk_bf16_f32 v197, v96, v97
	v_add_f32_e32 v212, v96, v212
	v_add_f32_e32 v212, v97, v212
	v_exp_f32_e32 v68, v68
	v_mfma_f32_32x32x16_bf16 v[98:113], v[244:247], v[174:177], v[98:113]
	v_exp_f32_e32 v69, v69
	v_cvt_pk_bf16_f32 v202, v66, v67
	v_add_f32_e32 v213, v66, v213
	v_add_f32_e32 v213, v67, v213
	s_waitcnt lgkmcnt(1)
	v_mfma_f32_32x32x16_bf16 v[18:33], v[216:219], v[178:181], v[18:33]
	ds_read_b128 v[240:243], v234 offset:38912
	v_exp_f32_e32 v70, v70
	v_exp_f32_e32 v71, v71
	v_cvt_pk_bf16_f32 v203, v68, v69
	v_add_f32_e32 v213, v68, v213
	s_waitcnt lgkmcnt(1)
	v_mfma_f32_32x32x16_bf16 v[34:49], v[220:223], v[178:181], v[34:49]
	ds_read_b128 v[244:247], v234 offset:39424
	v_add_f32_e32 v213, v69, v213
	v_exp_f32_e32 v72, v72
	v_exp_f32_e32 v73, v73
	v_mfma_f32_32x32x16_bf16 v[50:65], v[216:219], v[190:193], v[50:65]
	v_cvt_pk_bf16_f32 v204, v70, v71
	v_add_f32_e32 v213, v70, v213
	v_add_f32_e32 v213, v71, v213
	v_exp_f32_e32 v74, v74
	v_exp_f32_e32 v75, v75
	v_mfma_f32_32x32x16_bf16 v[2:17], v[220:223], v[190:193], v[2:17]
	v_cvt_pk_bf16_f32 v205, v72, v73
	v_add_f32_e32 v213, v72, v213
	v_add_f32_e32 v213, v73, v213
	v_exp_f32_e32 v76, v76
	s_waitcnt lgkmcnt(1)
	v_mfma_f32_32x32x16_bf16 v[18:33], v[240:243], v[182:185], v[18:33]
	ds_read_b128 v[216:219], v210 offset:20480
	v_exp_f32_e32 v77, v77
	v_cvt_pk_bf16_f32 v206, v74, v75
	v_add_f32_e32 v213, v74, v213
	v_add_f32_e32 v213, v75, v213
	s_waitcnt lgkmcnt(1)
	v_mfma_f32_32x32x16_bf16 v[34:49], v[244:247], v[182:185], v[34:49]
	v_exp_f32_e32 v78, v78
	v_exp_f32_e32 v79, v79
	v_cvt_pk_bf16_f32 v207, v76, v77
	v_add_f32_e32 v213, v76, v213
	v_mfma_f32_32x32x16_bf16 v[50:65], v[240:243], v[186:189], v[50:65]
	ds_read_b128 v[220:223], v210 offset:22528
	v_add_f32_e32 v213, v77, v213
	v_exp_f32_e32 v80, v80
	v_exp_f32_e32 v81, v81
	v_mfma_f32_32x32x16_bf16 v[2:17], v[244:247], v[186:189], v[2:17]
	v_cvt_pk_bf16_f32 v208, v78, v79
	v_add_f32_e32 v213, v78, v213
	v_add_f32_e32 v213, v79, v213
	v_cvt_pk_bf16_f32 v209, v80, v81
	v_add_f32_e32 v213, v80, v213
	v_add_f32_e32 v213, v81, v213
	s_waitcnt lgkmcnt(1)
	v_mfma_f32_32x32x16_bf16 v[82:97], v[216:219], v[130:133], 0
	ds_read_b128 v[240:243], v210 offset:24576
	v_exp_f32_e32 v114, v114
	v_exp_f32_e32 v115, v115
	v_exp_f32_e32 v116, v116
	v_mfma_f32_32x32x16_bf16 v[66:81], v[216:219], v[170:173], 0
	v_exp_f32_e32 v117, v117
	v_cvt_pk_bf16_f32 v178, v114, v115
	v_add_f32_e32 v212, v114, v212
	v_add_f32_e32 v212, v115, v212
	s_waitcnt lgkmcnt(1)
	v_mfma_f32_32x32x16_bf16 v[82:97], v[220:223], v[134:137], v[82:97]
	ds_read_b128 v[244:247], v210 offset:26624
	v_exp_f32_e32 v118, v118
	v_exp_f32_e32 v119, v119
	v_cvt_pk_bf16_f32 v179, v116, v117
	v_add_f32_e32 v212, v116, v212
	v_mfma_f32_32x32x16_bf16 v[66:81], v[220:223], v[138:141], v[66:81]
	v_add_f32_e32 v212, v117, v212
	v_exp_f32_e32 v120, v120
	v_exp_f32_e32 v121, v121
	s_waitcnt lgkmcnt(1)
	v_mfma_f32_32x32x16_bf16 v[82:97], v[240:243], v[146:149], v[82:97]
	ds_read_b128 v[216:219], v210 offset:28672
	v_cvt_pk_bf16_f32 v180, v118, v119
	v_add_f32_e32 v212, v118, v212
	v_add_f32_e32 v212, v119, v212
	v_exp_f32_e32 v122, v122
	v_exp_f32_e32 v123, v123
	v_mfma_f32_32x32x16_bf16 v[66:81], v[240:243], v[142:145], v[66:81]
	v_cvt_pk_bf16_f32 v181, v120, v121
	v_add_f32_e32 v212, v120, v212
	v_add_f32_e32 v212, v121, v212
	v_exp_f32_e32 v124, v124
	s_waitcnt lgkmcnt(1)
	v_mfma_f32_32x32x16_bf16 v[82:97], v[244:247], v[150:153], v[82:97]
	ds_read_b128 v[220:223], v210 offset:30720
	v_exp_f32_e32 v125, v125
	v_cvt_pk_bf16_f32 v182, v122, v123
	v_add_f32_e32 v212, v122, v212
	v_add_f32_e32 v212, v123, v212
	v_mfma_f32_32x32x16_bf16 v[66:81], v[244:247], v[154:157], v[66:81]
	v_exp_f32_e32 v126, v126
	v_exp_f32_e32 v127, v127
	v_cvt_pk_bf16_f32 v183, v124, v125
	v_add_f32_e32 v212, v124, v212
	s_waitcnt lgkmcnt(1)
	v_mfma_f32_32x32x16_bf16 v[82:97], v[216:219], v[162:165], v[82:97]
	ds_read_b128 v[240:243], v214 offset:12288
	v_add_f32_e32 v212, v125, v212
	v_exp_f32_e32 v128, v128
	v_exp_f32_e32 v129, v129
	v_mfma_f32_32x32x16_bf16 v[66:81], v[216:219], v[158:161], v[66:81]
	ds_read_b128 v[244:247], v214 offset:12800
	v_cvt_pk_bf16_f32 v184, v126, v127
	v_add_f32_e32 v212, v126, v212
	v_add_f32_e32 v212, v127, v212
	v_exp_f32_e32 v98, v98
	v_exp_f32_e32 v99, v99
	s_waitcnt lgkmcnt(2)
	v_mfma_f32_32x32x16_bf16 v[82:97], v[220:223], v[166:169], v[82:97]
	v_cvt_pk_bf16_f32 v185, v128, v129
	v_add_f32_e32 v212, v128, v212
	v_add_f32_e32 v212, v129, v212
	v_exp_f32_e32 v100, v100
	v_mfma_f32_32x32x16_bf16 v[66:81], v[220:223], v[174:177], v[66:81]
	v_exp_f32_e32 v101, v101
	v_cvt_pk_bf16_f32 v190, v98, v99
	v_add_f32_e32 v213, v98, v213
	v_add_f32_e32 v213, v99, v213
	s_waitcnt lgkmcnt(1)
	v_mfma_f32_32x32x16_bf16 v[18:33], v[240:243], v[198:201], v[18:33]
	ds_read_b128 v[216:219], v214 offset:14336
	v_exp_f32_e32 v102, v102
	v_exp_f32_e32 v103, v103
	v_cvt_pk_bf16_f32 v191, v100, v101
	v_add_f32_e32 v213, v100, v213
	s_waitcnt lgkmcnt(1)
	v_mfma_f32_32x32x16_bf16 v[34:49], v[244:247], v[198:201], v[34:49]
	ds_read_b128 v[220:223], v214 offset:14848
	v_add_f32_e32 v213, v101, v213
	v_exp_f32_e32 v104, v104
	v_exp_f32_e32 v105, v105
	v_mfma_f32_32x32x16_bf16 v[50:65], v[240:243], v[202:205], v[50:65]
	v_cvt_pk_bf16_f32 v192, v102, v103
	v_add_f32_e32 v213, v102, v213
	v_add_f32_e32 v213, v103, v213
	v_exp_f32_e32 v106, v106
	v_exp_f32_e32 v107, v107
	v_mfma_f32_32x32x16_bf16 v[2:17], v[244:247], v[202:205], v[2:17]
	v_cvt_pk_bf16_f32 v193, v104, v105
	v_add_f32_e32 v213, v104, v213
	v_add_f32_e32 v213, v105, v213
	v_exp_f32_e32 v108, v108
	s_waitcnt lgkmcnt(1)
	v_mfma_f32_32x32x16_bf16 v[18:33], v[216:219], v[194:197], v[18:33]
	ds_read_b128 v[240:243], v210 offset:20992
	v_exp_f32_e32 v109, v109
	v_cvt_pk_bf16_f32 v186, v106, v107
	v_add_f32_e32 v213, v106, v213
	v_add_f32_e32 v213, v107, v213
	s_waitcnt lgkmcnt(1)
	v_mfma_f32_32x32x16_bf16 v[34:49], v[220:223], v[194:197], v[34:49]
	v_exp_f32_e32 v110, v110
	v_exp_f32_e32 v111, v111
	v_cvt_pk_bf16_f32 v187, v108, v109
	v_add_f32_e32 v213, v108, v213
	v_mfma_f32_32x32x16_bf16 v[50:65], v[216:219], v[206:209], v[50:65]
	ds_read_b128 v[244:247], v210 offset:23040
	v_add_f32_e32 v213, v109, v213
	v_exp_f32_e32 v112, v112
	v_exp_f32_e32 v113, v113
	v_mfma_f32_32x32x16_bf16 v[2:17], v[220:223], v[206:209], v[2:17]
	v_cvt_pk_bf16_f32 v188, v110, v111
	v_add_f32_e32 v213, v110, v213
	v_add_f32_e32 v213, v111, v213
	v_cvt_pk_bf16_f32 v189, v112, v113
	v_add_f32_e32 v213, v112, v213
	v_add_f32_e32 v213, v113, v213
	s_waitcnt vmcnt(0)
	s_add_i32 s31, s31, 1
	s_waitcnt vmcnt(0) lgkmcnt(0)
	s_barrier
	s_min_i32 s34, s31, 0x101
	s_add_i32 s88, s34, 2
	s_mul_i32 s34, s88, 0x3000
	s_add_u32 s35, s22, s34
	s_addc_u32 s38, s23, 0
	s_add_u32 s40, s35, s25
	s_addc_u32 s41, s38, s26
	s_add_i32 s34, s27, 0x5000
	s_mov_b32 m0, s34
	s_andn2_b64 vcc, exec, s[10:11]
	global_load_lds_dwordx4 v0, s[40:41]
	s_cbranch_vccnz .Lmla929_3
	s_add_u32 s40, s35, s28
	s_addc_u32 s41, s38, s29
	s_add_i32 m0, s34, 0x2000
	s_nop 0
	global_load_lds_dwordx4 v0, s[40:41]
.Lmla929_3:
	s_lshl_b64 s[38:39], s[88:89], 13
	s_add_i32 m0, s34, 0x3000
	s_add_u32 s60, s56, s38
	s_addc_u32 s61, s57, s39
	global_load_lds_dwordx4 v0, s[60:61]
	ds_read_b128 v[216:219], v224 offset:25088
	v_mfma_f32_32x32x16_bf16 v[114:129], v[240:243], v[130:133], 0
	v_exp_f32_e32 v82, v82
	v_exp_f32_e32 v83, v83
	v_exp_f32_e32 v84, v84
	v_mfma_f32_32x32x16_bf16 v[98:113], v[240:243], v[170:173], 0
	ds_read_b128 v[220:223], v224 offset:27136
	v_exp_f32_e32 v85, v85
	v_cvt_pk_bf16_f32 v198, v82, v83
	v_add_f32_e32 v212, v82, v212
	v_add_f32_e32 v212, v83, v212
	v_mfma_f32_32x32x16_bf16 v[114:129], v[244:247], v[134:137], v[114:129]
	v_exp_f32_e32 v86, v86
	v_exp_f32_e32 v87, v87
	v_cvt_pk_bf16_f32 v199, v84, v85
	v_add_f32_e32 v212, v84, v212
	v_mfma_f32_32x32x16_bf16 v[98:113], v[244:247], v[138:141], v[98:113]
	ds_read_b128 v[240:243], v224 offset:29184
	v_add_f32_e32 v212, v85, v212
	v_exp_f32_e32 v88, v88
	v_exp_f32_e32 v89, v89
	s_waitcnt lgkmcnt(2)
	v_mfma_f32_32x32x16_bf16 v[114:129], v[216:219], v[146:149], v[114:129]
	v_cvt_pk_bf16_f32 v200, v86, v87
	v_add_f32_e32 v212, v86, v212
	v_add_f32_e32 v212, v87, v212
	v_exp_f32_e32 v90, v90
	v_exp_f32_e32 v91, v91
	v_mfma_f32_32x32x16_bf16 v[98:113], v[216:219], v[142:145], v[98:113]
	ds_read_b128 v[244:247], v224 offset:31232
	v_cvt_pk_bf16_f32 v201, v88, v89
	v_add_f32_e32 v212, v88, v212
	v_add_f32_e32 v212, v89, v212
	v_exp_f32_e32 v92, v92
	s_waitcnt lgkmcnt(2)
	v_mfma_f32_32x32x16_bf16 v[114:129], v[220:223], v[150:153], v[114:129]
	v_exp_f32_e32 v93, v93
	v_cvt_pk_bf16_f32 v194, v90, v91
	v_add_f32_e32 v212, v90, v212
	v_add_f32_e32 v212, v91, v212
	v_mfma_f32_32x32x16_bf16 v[98:113], v[220:223], v[154:157], v[98:113]
	ds_read_b128 v[216:219], v215 offset:16384
	v_exp_f32_e32 v94, v94
	v_exp_f32_e32 v95, v95
	v_cvt_pk_bf16_f32 v195, v92, v93
	v_add_f32_e32 v212, v92, v212
	s_waitcnt lgkmcnt(2)
	v_mfma_f32_32x32x16_bf16 v[114:129], v[240:243], v[162:165], v[114:129]
	v_add_f32_e32 v212, v93, v212
	v_exp_f32_e32 v96, v96
	v_exp_f32_e32 v97, v97
	v_mfma_f32_32x32x16_bf16 v[98:113], v[240:243], v[158:161], v[98:113]
	ds_read_b128 v[220:223], v215 offset:16896
	v_cvt_pk_bf16_f32 v196, v94, v95
	v_add_f32_e32 v212, v94, v212
	v_add_f32_e32 v212, v95, v212
	v_exp_f32_e32 v66, v66
	v_exp_f32_e32 v67, v67
	s_waitcnt lgkmcnt(2)
	v_mfma_f32_32x32x16_bf16 v[114:129], v[244:247], v[166:169], v[114:129]
	v_cvt_pk_bf16_f32 v197, v96, v97
	v_add_f32_e32 v212, v96, v212
	v_add_f32_e32 v212, v97, v212
	v_exp_f32_e32 v68, v68
	v_mfma_f32_32x32x16_bf16 v[98:113], v[244:247], v[174:177], v[98:113]
	v_exp_f32_e32 v69, v69
	v_cvt_pk_bf16_f32 v202, v66, v67
	v_add_f32_e32 v213, v66, v213
	v_add_f32_e32 v213, v67, v213
	s_waitcnt lgkmcnt(1)
	v_mfma_f32_32x32x16_bf16 v[18:33], v[216:219], v[178:181], v[18:33]
	ds_read_b128 v[240:243], v215 offset:18432
	v_exp_f32_e32 v70, v70
	v_exp_f32_e32 v71, v71
	v_cvt_pk_bf16_f32 v203, v68, v69
	v_add_f32_e32 v213, v68, v213
	s_waitcnt lgkmcnt(1)
	v_mfma_f32_32x32x16_bf16 v[34:49], v[220:223], v[178:181], v[34:49]
	ds_read_b128 v[244:247], v215 offset:18944
	v_add_f32_e32 v213, v69, v213
	v_exp_f32_e32 v72, v72
	v_exp_f32_e32 v73, v73
	v_mfma_f32_32x32x16_bf16 v[50:65], v[216:219], v[190:193], v[50:65]
	v_cvt_pk_bf16_f32 v204, v70, v71
	v_add_f32_e32 v213, v70, v213
	v_add_f32_e32 v213, v71, v213
	v_exp_f32_e32 v74, v74
	v_exp_f32_e32 v75, v75
	v_mfma_f32_32x32x16_bf16 v[2:17], v[220:223], v[190:193], v[2:17]
	v_cvt_pk_bf16_f32 v205, v72, v73
	v_add_f32_e32 v213, v72, v213
	v_add_f32_e32 v213, v73, v213
	v_exp_f32_e32 v76, v76
	s_waitcnt lgkmcnt(1)
	v_mfma_f32_32x32x16_bf16 v[18:33], v[240:243], v[182:185], v[18:33]
	ds_read_b128 v[216:219], v232 offset:0
	v_exp_f32_e32 v77, v77
	v_cvt_pk_bf16_f32 v206, v74, v75
	v_add_f32_e32 v213, v74, v213
	v_add_f32_e32 v213, v75, v213
	s_waitcnt lgkmcnt(1)
	v_mfma_f32_32x32x16_bf16 v[34:49], v[244:247], v[182:185], v[34:49]
	v_exp_f32_e32 v78, v78
	v_exp_f32_e32 v79, v79
	v_cvt_pk_bf16_f32 v207, v76, v77
	v_add_f32_e32 v213, v76, v213
	v_mfma_f32_32x32x16_bf16 v[50:65], v[240:243], v[186:189], v[50:65]
	ds_read_b128 v[220:223], v232 offset:2048
	v_add_f32_e32 v213, v77, v213
	v_exp_f32_e32 v80, v80
	v_exp_f32_e32 v81, v81
	v_mfma_f32_32x32x16_bf16 v[2:17], v[244:247], v[186:189], v[2:17]
	v_cvt_pk_bf16_f32 v208, v78, v79
	v_add_f32_e32 v213, v78, v213
	v_add_f32_e32 v213, v79, v213
	v_cvt_pk_bf16_f32 v209, v80, v81
	v_add_f32_e32 v213, v80, v213
	v_add_f32_e32 v213, v81, v213
	s_waitcnt lgkmcnt(1)
	v_mfma_f32_32x32x16_bf16 v[82:97], v[216:219], v[130:133], 0
	ds_read_b128 v[240:243], v232 offset:4096
	v_exp_f32_e32 v114, v114
	v_exp_f32_e32 v115, v115
	v_exp_f32_e32 v116, v116
	v_mfma_f32_32x32x16_bf16 v[66:81], v[216:219], v[170:173], 0
	v_exp_f32_e32 v117, v117
	v_cvt_pk_bf16_f32 v178, v114, v115
	v_add_f32_e32 v212, v114, v212
	v_add_f32_e32 v212, v115, v212
	s_waitcnt lgkmcnt(1)
	v_mfma_f32_32x32x16_bf16 v[82:97], v[220:223], v[134:137], v[82:97]
	ds_read_b128 v[244:247], v232 offset:6144
	v_exp_f32_e32 v118, v118
	v_exp_f32_e32 v119, v119
	v_cvt_pk_bf16_f32 v179, v116, v117
	v_add_f32_e32 v212, v116, v212
	v_mfma_f32_32x32x16_bf16 v[66:81], v[220:223], v[138:141], v[66:81]
	v_add_f32_e32 v212, v117, v212
	v_exp_f32_e32 v120, v120
	v_exp_f32_e32 v121, v121
	s_waitcnt lgkmcnt(1)
	v_mfma_f32_32x32x16_bf16 v[82:97], v[240:243], v[146:149], v[82:97]
	ds_read_b128 v[216:219], v232 offset:8192
	v_cvt_pk_bf16_f32 v180, v118, v119
	v_add_f32_e32 v212, v118, v212
	v_add_f32_e32 v212, v119, v212
	v_exp_f32_e32 v122, v122
	v_exp_f32_e32 v123, v123
	v_mfma_f32_32x32x16_bf16 v[66:81], v[240:243], v[142:145], v[66:81]
	v_cvt_pk_bf16_f32 v181, v120, v121
	v_add_f32_e32 v212, v120, v212
	v_add_f32_e32 v212, v121, v212
	v_exp_f32_e32 v124, v124
	s_waitcnt lgkmcnt(1)
	v_mfma_f32_32x32x16_bf16 v[82:97], v[244:247], v[150:153], v[82:97]
	ds_read_b128 v[220:223], v232 offset:10240
	v_exp_f32_e32 v125, v125
	v_cvt_pk_bf16_f32 v182, v122, v123
	v_add_f32_e32 v212, v122, v212
	v_add_f32_e32 v212, v123, v212
	v_mfma_f32_32x32x16_bf16 v[66:81], v[244:247], v[154:157], v[66:81]
	v_exp_f32_e32 v126, v126
	v_exp_f32_e32 v127, v127
	v_cvt_pk_bf16_f32 v183, v124, v125
	v_add_f32_e32 v212, v124, v212
	s_waitcnt lgkmcnt(1)
	v_mfma_f32_32x32x16_bf16 v[82:97], v[216:219], v[162:165], v[82:97]
	ds_read_b128 v[240:243], v214 offset:32768
	v_add_f32_e32 v212, v125, v212
	v_exp_f32_e32 v128, v128
	v_exp_f32_e32 v129, v129
	v_mfma_f32_32x32x16_bf16 v[66:81], v[216:219], v[158:161], v[66:81]
	ds_read_b128 v[244:247], v214 offset:33280
	v_cvt_pk_bf16_f32 v184, v126, v127
	v_add_f32_e32 v212, v126, v212
	v_add_f32_e32 v212, v127, v212
	v_exp_f32_e32 v98, v98
	v_exp_f32_e32 v99, v99
	s_waitcnt lgkmcnt(2)
	v_mfma_f32_32x32x16_bf16 v[82:97], v[220:223], v[166:169], v[82:97]
	v_cvt_pk_bf16_f32 v185, v128, v129
	v_add_f32_e32 v212, v128, v212
	v_add_f32_e32 v212, v129, v212
	v_exp_f32_e32 v100, v100
	v_mfma_f32_32x32x16_bf16 v[66:81], v[220:223], v[174:177], v[66:81]
	v_exp_f32_e32 v101, v101
	v_cvt_pk_bf16_f32 v190, v98, v99
	v_add_f32_e32 v213, v98, v213
	v_add_f32_e32 v213, v99, v213
	s_waitcnt lgkmcnt(1)
	v_mfma_f32_32x32x16_bf16 v[18:33], v[240:243], v[198:201], v[18:33]
	ds_read_b128 v[216:219], v214 offset:34816
	v_exp_f32_e32 v102, v102
	v_exp_f32_e32 v103, v103
	v_cvt_pk_bf16_f32 v191, v100, v101
	v_add_f32_e32 v213, v100, v213
	s_waitcnt lgkmcnt(1)
	v_mfma_f32_32x32x16_bf16 v[34:49], v[244:247], v[198:201], v[34:49]
	ds_read_b128 v[220:223], v214 offset:35328
	v_add_f32_e32 v213, v101, v213
	v_exp_f32_e32 v104, v104
	v_exp_f32_e32 v105, v105
	v_mfma_f32_32x32x16_bf16 v[50:65], v[240:243], v[202:205], v[50:65]
	v_cvt_pk_bf16_f32 v192, v102, v103
	v_add_f32_e32 v213, v102, v213
	v_add_f32_e32 v213, v103, v213
	v_exp_f32_e32 v106, v106
	v_exp_f32_e32 v107, v107
	v_mfma_f32_32x32x16_bf16 v[2:17], v[244:247], v[202:205], v[2:17]
	v_cvt_pk_bf16_f32 v193, v104, v105
	v_add_f32_e32 v213, v104, v213
	v_add_f32_e32 v213, v105, v213
	v_exp_f32_e32 v108, v108
	s_waitcnt lgkmcnt(1)
	v_mfma_f32_32x32x16_bf16 v[18:33], v[216:219], v[194:197], v[18:33]
	ds_read_b128 v[240:243], v232 offset:512
	v_exp_f32_e32 v109, v109
	v_cvt_pk_bf16_f32 v186, v106, v107
	v_add_f32_e32 v213, v106, v213
	v_add_f32_e32 v213, v107, v213
	s_waitcnt lgkmcnt(1)
	v_mfma_f32_32x32x16_bf16 v[34:49], v[220:223], v[194:197], v[34:49]
	v_exp_f32_e32 v110, v110
	v_exp_f32_e32 v111, v111
	v_cvt_pk_bf16_f32 v187, v108, v109
	v_add_f32_e32 v213, v108, v213
	v_mfma_f32_32x32x16_bf16 v[50:65], v[216:219], v[206:209], v[50:65]
	ds_read_b128 v[244:247], v232 offset:2560
	v_add_f32_e32 v213, v109, v213
	v_exp_f32_e32 v112, v112
	v_exp_f32_e32 v113, v113
	v_mfma_f32_32x32x16_bf16 v[2:17], v[220:223], v[206:209], v[2:17]
	v_cvt_pk_bf16_f32 v188, v110, v111
	v_add_f32_e32 v213, v110, v213
	v_add_f32_e32 v213, v111, v213
	v_cvt_pk_bf16_f32 v189, v112, v113
	v_add_f32_e32 v213, v112, v213
	v_add_f32_e32 v213, v113, v213
	s_waitcnt vmcnt(0)
	s_add_i32 s31, s31, 1
	s_cmpk_eq_i32 s31, 0x104
	s_waitcnt vmcnt(0) lgkmcnt(0)
	s_barrier
	s_cbranch_scc1 .LBB0_931
	s_mov_b32 s33, 3
	s_branch .LBB0_927
.LBB0_931:
	v_add_u32_e32 v235, 0xf000, v233
	v_mov_b32_e32 v202, v212
	v_mov_b32_e32 v203, v213
	ds_read_b128 v[66:69], v235 offset:16384
	ds_read_b128 v[70:73], v235 offset:16896
	v_mov_b32_e32 v0, v230
	s_movk_i32 s54, 0x6000
	v_mov_b32_e32 v224, 0x358637bd
	s_waitcnt lgkmcnt(1)
	v_mfma_f32_32x32x16_bf16 v[18:33], v[66:69], v[178:181], v[18:33]
	s_waitcnt lgkmcnt(0)
	v_mfma_f32_32x32x16_bf16 v[34:49], v[70:73], v[178:181], v[34:49]
	v_mfma_f32_32x32x16_bf16 v[50:65], v[66:69], v[190:193], v[50:65]
	v_mfma_f32_32x32x16_bf16 v[2:17], v[70:73], v[190:193], v[2:17]
	ds_read_b128 v[66:69], v235 offset:18432
	ds_read_b128 v[70:73], v235 offset:18944
	s_nop 0
	v_readfirstlane_b32 s10, v0
	s_andn2_b32 s10, s10, 63
	s_cmpk_lt_i32 s10, 0x200
	s_waitcnt lgkmcnt(1)
	v_mfma_f32_32x32x16_bf16 v[18:33], v[66:69], v[182:185], v[18:33]
	s_waitcnt lgkmcnt(0)
	v_mfma_f32_32x32x16_bf16 v[34:49], v[70:73], v[182:185], v[34:49]
	v_mfma_f32_32x32x16_bf16 v[50:65], v[66:69], v[186:189], v[50:65]
	v_mbcnt_lo_u32_b32 v66, -1, 0
	v_mbcnt_hi_u32_b32 v66, -1, v66
	v_mbcnt_lo_u32_b32 v67, -1, 0
	v_mbcnt_hi_u32_b32 v67, -1, v67
	s_nop 0
	v_lshlrev_b32_e32 v66, 2, v66
	v_lshlrev_b32_e32 v67, 2, v67
	v_xor_b32_e32 v66, 0x80, v66
	v_xor_b32_e32 v67, 0x80, v67
	v_mfma_f32_32x32x16_bf16 v[2:17], v[70:73], v[186:189], v[2:17]
	ds_bpermute_b32 v66, v66, v202
	ds_bpermute_b32 v67, v67, v203
	s_cbranch_scc0 .LBB0_919
	s_lshl_b64 s[6:7], s[6:7], 11
	s_waitcnt lgkmcnt(1)
	v_add_f32_e32 v66, v202, v66
	s_add_u32 s6, s2, s6
	v_rcp_f32_e32 v66, v66
	s_addc_u32 s7, s3, s7
	s_lshl_b32 s11, s21, 7
	v_and_or_b32 v68, v0, 31, s10
	s_add_u32 s6, s6, s11
	v_ashrrev_i32_e32 v69, 31, v68
	s_addc_u32 s7, s7, 0
	s_waitcnt lgkmcnt(0)
	v_add_f32_e32 v67, v203, v67
	v_lshlrev_b64 v[68:69], 11, v[68:69]
	v_lshrrev_b32_e32 v0, 2, v0
	v_lshl_add_u64 v[68:69], s[6:7], 0, v[68:69]
	v_pk_mul_f32 v[18:19], v[18:19], v[66:67] op_sel_hi:[1,0]
	v_pk_mul_f32 v[20:21], v[20:21], v[66:67] op_sel_hi:[1,0]
	v_and_b32_e32 v0, 8, v0
	v_rcp_f32_e32 v70, v67
	v_pk_mul_f32 v[34:35], v[34:35], v[66:67] op_sel_hi:[1,0]
	v_pk_mul_f32 v[36:37], v[36:37], v[66:67] op_sel_hi:[1,0]
	v_pk_mul_f32 v[38:39], v[38:39], v[66:67] op_sel_hi:[1,0]
	v_pk_mul_f32 v[40:41], v[40:41], v[66:67] op_sel_hi:[1,0]
	v_pk_mul_f32 v[42:43], v[42:43], v[66:67] op_sel_hi:[1,0]
	v_pk_mul_f32 v[44:45], v[44:45], v[66:67] op_sel_hi:[1,0]
	v_pk_mul_f32 v[46:47], v[46:47], v[66:67] op_sel_hi:[1,0]
	v_pk_mul_f32 v[48:49], v[48:49], v[66:67] op_sel_hi:[1,0]
	v_pk_mul_f32 v[22:23], v[22:23], v[66:67] op_sel_hi:[1,0]
	v_pk_mul_f32 v[24:25], v[24:25], v[66:67] op_sel_hi:[1,0]
	v_pk_mul_f32 v[26:27], v[26:27], v[66:67] op_sel_hi:[1,0]
	v_pk_mul_f32 v[28:29], v[28:29], v[66:67] op_sel_hi:[1,0]
	v_pk_mul_f32 v[30:31], v[30:31], v[66:67] op_sel_hi:[1,0]
	v_pk_mul_f32 v[32:33], v[32:33], v[66:67] op_sel_hi:[1,0]
	v_lshl_add_u64 v[66:67], v[68:69], 0, v[0:1]
	v_cvt_pk_bf16_f32 v18, v18, v19
	v_cvt_pk_bf16_f32 v19, v20, v21
	v_cvt_pk_bf16_f32 v20, v34, v35
	v_cvt_pk_bf16_f32 v21, v36, v37
	global_store_dwordx2 v[66:67], v[18:19], off offset:512
	global_store_dwordx2 v[66:67], v[20:21], off offset:576
	v_cvt_pk_bf16_f32 v18, v22, v23
	v_cvt_pk_bf16_f32 v19, v24, v25
	v_cvt_pk_bf16_f32 v20, v38, v39
	v_cvt_pk_bf16_f32 v21, v40, v41
	global_store_dwordx2 v[66:67], v[18:19], off offset:528
	global_store_dwordx2 v[66:67], v[20:21], off offset:592
	v_cvt_pk_bf16_f32 v18, v26, v27
	v_cvt_pk_bf16_f32 v19, v28, v29
	v_cvt_pk_bf16_f32 v20, v42, v43
	v_cvt_pk_bf16_f32 v21, v44, v45
	global_store_dwordx2 v[66:67], v[18:19], off offset:544
	global_store_dwordx2 v[66:67], v[20:21], off offset:608
	v_cvt_pk_bf16_f32 v18, v30, v31
	v_cvt_pk_bf16_f32 v19, v32, v33
	s_mov_b64 s[6:7], 0x10200
	v_cvt_pk_bf16_f32 v20, v46, v47
	v_cvt_pk_bf16_f32 v21, v48, v49
	global_store_dwordx2 v[66:67], v[18:19], off offset:560
	global_store_dwordx2 v[66:67], v[20:21], off offset:624
	v_lshl_add_u64 v[18:19], v[66:67], 0, s[6:7]
	s_mov_b64 s[6:7], 0x10240
	v_pk_mul_f32 v[2:3], v[2:3], v[70:71] op_sel_hi:[1,0]
	v_pk_mul_f32 v[4:5], v[4:5], v[70:71] op_sel_hi:[1,0]
	v_lshl_add_u64 v[20:21], v[66:67], 0, s[6:7]
	s_mov_b32 s6, 0x10000
	v_pk_mul_f32 v[50:51], v[50:51], v[70:71] op_sel_hi:[1,0]
	v_pk_mul_f32 v[52:53], v[52:53], v[70:71] op_sel_hi:[1,0]
	v_cvt_pk_bf16_f32 v2, v2, v3
	v_cvt_pk_bf16_f32 v3, v4, v5
	v_add_co_u32_e32 v4, vcc, s6, v66
	v_pk_mul_f32 v[54:55], v[54:55], v[70:71] op_sel_hi:[1,0]
	v_pk_mul_f32 v[56:57], v[56:57], v[70:71] op_sel_hi:[1,0]
	v_cvt_pk_bf16_f32 v22, v50, v51
	v_cvt_pk_bf16_f32 v23, v52, v53
	v_addc_co_u32_e32 v5, vcc, 0, v67, vcc
	v_pk_mul_f32 v[6:7], v[6:7], v[70:71] op_sel_hi:[1,0]
	v_pk_mul_f32 v[8:9], v[8:9], v[70:71] op_sel_hi:[1,0]
	v_pk_mul_f32 v[58:59], v[58:59], v[70:71] op_sel_hi:[1,0]
	v_pk_mul_f32 v[60:61], v[60:61], v[70:71] op_sel_hi:[1,0]
	global_store_dwordx2 v[4:5], v[22:23], off offset:512
	global_store_dwordx2 v[4:5], v[2:3], off offset:576
	v_cvt_pk_bf16_f32 v2, v54, v55
	v_cvt_pk_bf16_f32 v3, v56, v57
	v_pk_mul_f32 v[10:11], v[10:11], v[70:71] op_sel_hi:[1,0]
	v_pk_mul_f32 v[12:13], v[12:13], v[70:71] op_sel_hi:[1,0]
	v_pk_mul_f32 v[62:63], v[62:63], v[70:71] op_sel_hi:[1,0]
	v_pk_mul_f32 v[64:65], v[64:65], v[70:71] op_sel_hi:[1,0]
	v_cvt_pk_bf16_f32 v4, v6, v7
	v_cvt_pk_bf16_f32 v5, v8, v9
	global_store_dwordx2 v[18:19], v[2:3], off offset:16
	global_store_dwordx2 v[20:21], v[4:5], off offset:16
	v_cvt_pk_bf16_f32 v2, v58, v59
	v_cvt_pk_bf16_f32 v3, v60, v61
	v_pk_mul_f32 v[14:15], v[14:15], v[70:71] op_sel_hi:[1,0]
	v_pk_mul_f32 v[16:17], v[16:17], v[70:71] op_sel_hi:[1,0]
	v_cvt_pk_bf16_f32 v4, v10, v11
	v_cvt_pk_bf16_f32 v5, v12, v13
	global_store_dwordx2 v[18:19], v[2:3], off offset:32
	global_store_dwordx2 v[20:21], v[4:5], off offset:32
	v_cvt_pk_bf16_f32 v2, v62, v63
	v_cvt_pk_bf16_f32 v3, v64, v65
	v_cvt_pk_bf16_f32 v4, v14, v15
	v_cvt_pk_bf16_f32 v5, v16, v17
	global_store_dwordx2 v[18:19], v[2:3], off offset:48
	global_store_dwordx2 v[20:21], v[4:5], off offset:48
	s_branch .LBB0_919
